# combine: LayerNorm gamma/beta preloaded once per phase; their per-row loads and drain waits removed
# baseline (speedup 1.0000x reference)
.LBB0_1512:
	s_cmp_le_i32 s74, s2
	s_cselect_b64 s[8:9], -1, 0
	s_and_b64 s[2:3], s[8:9], s[0:1]
	s_andn2_b64 vcc, exec, s[2:3]
	s_cbranch_vccnz .LBB0_1533
	v_readlane_b32 s2, v254, 41
	v_readlane_b32 s3, v254, 57
	v_readlane_b32 s14, v254, 14
	v_mov_b32_e32 v0, s2
	s_waitcnt vmcnt(0)
	ds_read_b64 v[2:3], v0
	v_mbcnt_lo_u32_b32 v0, -1, 0
	v_mbcnt_hi_u32_b32 v0, -1, v0
	v_readlane_b32 s2, v253, 0
	v_mov_b32_e32 v6, s3
	s_waitcnt lgkmcnt(0)
	v_readfirstlane_b32 s12, v2
	v_add_u32_e32 v0, s2, v0
	v_readlane_b32 s2, v254, 56
	v_readfirstlane_b32 s13, v3
	ds_read_b64 v[6:7], v6
	v_mov_b32_e32 v2, s2
	ds_read_b128 v[2:5], v2
	v_readfirstlane_b32 s2, v0
	s_ashr_i32 s2, s2, 6
	s_add_i32 s14, s2, s14
	s_waitcnt lgkmcnt(1)
	v_readfirstlane_b32 s16, v6
	s_waitcnt lgkmcnt(0)
	v_readfirstlane_b32 s3, v2
	v_readfirstlane_b32 s11, v3
	v_readfirstlane_b32 s15, v4
	v_readfirstlane_b32 s18, v5
	s_cmpk_lt_i32 s14, 0x4000
	v_readfirstlane_b32 s17, v7
	s_cbranch_scc0 .LBB0_1533
	v_readlane_b32 s26, v253, 3
	v_readlane_b32 s27, v253, 4
	s_load_dword s25, s[26:27], 0x0
	v_readlane_b32 s26, v254, 60
	v_readlane_b32 s27, v254, 61
	s_lshl_b32 s56, s26, 10
	s_lshl_b64 s[26:27], s[56:57], 2
	s_waitcnt lgkmcnt(0)
	s_lshl_b32 s2, s25, 3
	s_add_u32 s28, s15, s26
	s_addc_u32 s29, s18, s27
	s_add_u32 s18, s3, s26
	s_addc_u32 s19, s11, s27
	s_add_u32 s26, s12, 0x20000
	s_addc_u32 s27, s13, 0
	s_ashr_i32 s15, s14, 31
	s_lshl_b64 s[30:31], s[14:15], 11
	s_add_u32 s34, s26, s30
	s_addc_u32 s35, s27, s31
	s_add_u32 s36, s12, 0x43be0200
	v_lshlrev_b32_e32 v0, 3, v0
	s_addc_u32 s37, s13, 0
	v_and_b32_e32 v0, 0x1f8, v0
	s_add_u32 s30, s36, s30
	v_lshlrev_b32_e32 v18, 1, v0
	s_addc_u32 s31, s37, s31
	global_load_dwordx4 v[6:9], v18, s[34:35] offset:1024
	global_load_dwordx4 v[14:17], v18, s[34:35]
	global_load_dwordx4 v[2:5], v18, s[30:31] offset:1024
	global_load_dwordx4 v[10:13], v18, s[30:31]
	s_add_u32 s30, s12, 0x33be0200
	s_addc_u32 s31, s13, 0
	s_lshl_b64 s[34:35], s[14:15], 13
	s_add_u32 s34, s30, s34
	s_addc_u32 s35, s31, s35
	v_lshl_add_u64 v[20:21], s[34:35], 0, v[0:1]
	v_add_co_u32_e32 v20, vcc, s85, v20
	v_mov_b32_e32 v19, v1
	s_nop 0
	v_addc_co_u32_e32 v21, vcc, 0, v21, vcc
	global_load_dwordx2 v[48:49], v[20:21], off offset:3584
	global_load_dwordx2 v[50:51], v[20:21], off offset:3072
	global_load_dwordx2 v[52:53], v[20:21], off offset:2560
	global_load_dwordx2 v[54:55], v[20:21], off offset:2048
	global_load_dwordx2 v[56:57], v[20:21], off offset:1536
	global_load_dwordx2 v[58:59], v[20:21], off offset:1024
	global_load_dwordx2 v[60:61], v[20:21], off offset:512
	global_load_dwordx2 v[64:65], v[20:21], off
	global_load_dwordx2 v[62:63], v0, s[34:35] offset:3584
	global_load_dwordx2 v[66:67], v0, s[34:35] offset:3072
	global_load_dwordx2 v[68:69], v0, s[34:35] offset:2560
	global_load_dwordx2 v[70:71], v0, s[34:35] offset:2048
	global_load_dwordx2 v[72:73], v0, s[34:35] offset:1536
	global_load_dwordx2 v[74:75], v0, s[34:35] offset:1024
	global_load_dwordx2 v[76:77], v0, s[34:35] offset:512
	global_load_dwordx2 v[84:85], v0, s[34:35]
	v_lshl_add_u64 v[36:37], s[36:37], 0, v[18:19]
	v_lshl_add_u64 v[38:39], s[26:27], 0, v[18:19]
	v_lshlrev_b32_e32 v18, 2, v0
	v_lshl_add_u64 v[40:41], s[18:19], 0, v[18:19]
	v_lshl_add_u64 v[42:43], s[28:29], 0, v[18:19]
	global_load_dwordx4 v[192:195], v[40:41], off
	global_load_dwordx4 v[196:199], v[40:41], off offset:16
	global_load_dwordx4 v[200:203], v[40:41], off offset:2048
	global_load_dwordx4 v[204:207], v[40:41], off offset:2064
	global_load_dwordx4 v[208:211], v[42:43], off
	global_load_dwordx4 v[212:215], v[42:43], off offset:16
	global_load_dwordx4 v[216:219], v[42:43], off offset:2048
	global_load_dwordx4 v[240:243], v[42:43], off offset:2064
	v_lshl_add_u64 v[44:45], s[16:17], 0, v[18:19]
	v_lshl_add_u64 v[18:19], s[12:13], 0, v[0:1]
	s_mov_b64 s[12:13], 0x519e0a00
	v_lshl_add_u64 v[34:35], s[30:31], 0, v[0:1]
	v_lshl_add_u64 v[46:47], v[18:19], 0, s[12:13]
	s_lshl_b32 s3, s25, 4
	s_branch .LBB0_1516

.LBB0_1516:
	s_waitcnt vmcnt(0)
	v_cvt_pk_f32_fp8_sdwa v[114:115], v84 src0_sel:WORD_1
	v_cvt_pk_f32_fp8_e32 v[112:113], v84
	v_lshlrev_b32_e32 v116, 16, v14
	v_and_b32_e32 v117, 0xffff0000, v14
	v_lshlrev_b32_e32 v118, 16, v10
	v_and_b32_e32 v119, 0xffff0000, v10
	v_lshlrev_b32_e32 v14, 16, v15
	v_and_b32_e32 v15, 0xffff0000, v15
	v_lshlrev_b32_e32 v10, 16, v11
	v_and_b32_e32 v11, 0xffff0000, v11
	v_pk_fma_f32 v[10:11], v[14:15], s[10:11], v[10:11] op_sel_hi:[1,0,1]
	v_pk_fma_f32 v[116:117], v[116:117], s[10:11], v[118:119] op_sel_hi:[1,0,1]
	v_pk_fma_f32 v[14:15], v[114:115], s[24:25], v[10:11] op_sel_hi:[1,0,1]
	v_cvt_pk_f32_fp8_e32 v[10:11], v85
	v_pk_fma_f32 v[112:113], v[112:113], s[24:25], v[116:117] op_sel_hi:[1,0,1]
	v_cvt_pk_f32_fp8_sdwa v[84:85], v85 src0_sel:WORD_1
	v_lshlrev_b32_e32 v114, 16, v16
	v_and_b32_e32 v115, 0xffff0000, v16
	v_lshlrev_b32_e32 v116, 16, v12
	v_and_b32_e32 v117, 0xffff0000, v12
	v_pk_fma_f32 v[114:115], v[114:115], s[10:11], v[116:117] op_sel_hi:[1,0,1]
	v_lshlrev_b32_e32 v12, 16, v13
	v_pk_fma_f32 v[114:115], v[10:11], s[24:25], v[114:115] op_sel_hi:[1,0,1]
	v_lshlrev_b32_e32 v10, 16, v17
	v_and_b32_e32 v11, 0xffff0000, v17
	v_and_b32_e32 v13, 0xffff0000, v13
	v_pk_fma_f32 v[10:11], v[10:11], s[10:11], v[12:13] op_sel_hi:[1,0,1]
	v_cvt_pk_f32_fp8_sdwa v[16:17], v76 src0_sel:WORD_1
	v_pk_fma_f32 v[12:13], v[84:85], s[24:25], v[10:11] op_sel_hi:[1,0,1]
	v_cvt_pk_f32_fp8_e32 v[10:11], v76
	v_lshlrev_b32_e32 v84, 16, v6
	v_and_b32_e32 v85, 0xffff0000, v6
	v_lshlrev_b32_e32 v116, 16, v2
	v_and_b32_e32 v117, 0xffff0000, v2
	v_lshlrev_b32_e32 v6, 16, v7
	v_and_b32_e32 v7, 0xffff0000, v7
	v_lshlrev_b32_e32 v2, 16, v3
	v_and_b32_e32 v3, 0xffff0000, v3
	v_pk_fma_f32 v[84:85], v[84:85], s[10:11], v[116:117] op_sel_hi:[1,0,1]
	v_pk_fma_f32 v[2:3], v[6:7], s[10:11], v[2:3] op_sel_hi:[1,0,1]
	v_pk_fma_f32 v[10:11], v[10:11], s[24:25], v[84:85] op_sel_hi:[1,0,1]
	v_pk_fma_f32 v[2:3], v[16:17], s[24:25], v[2:3] op_sel_hi:[1,0,1]
	v_cvt_pk_f32_fp8_e32 v[6:7], v77
	v_cvt_pk_f32_fp8_sdwa v[16:17], v77 src0_sel:WORD_1
	v_lshlrev_b32_e32 v76, 16, v8
	v_and_b32_e32 v77, 0xffff0000, v8
	v_lshlrev_b32_e32 v84, 16, v4
	v_and_b32_e32 v85, 0xffff0000, v4
	v_lshlrev_b32_e32 v8, 16, v9
	v_and_b32_e32 v9, 0xffff0000, v9
	v_lshlrev_b32_e32 v4, 16, v5
	v_and_b32_e32 v5, 0xffff0000, v5
	v_cvt_pk_f32_fp8_sdwa v[116:117], v72 src0_sel:WORD_1
	v_pk_fma_f32 v[4:5], v[8:9], s[10:11], v[4:5] op_sel_hi:[1,0,1]
	v_cvt_pk_f32_fp8_e32 v[8:9], v72
	v_cvt_pk_f32_fp8_e32 v[118:119], v73
	v_cvt_pk_f32_fp8_sdwa v[72:73], v73 src0_sel:WORD_1
	v_cvt_pk_f32_fp8_sdwa v[128:129], v68 src0_sel:WORD_1
	v_cvt_pk_f32_fp8_e32 v[126:127], v68
	v_cvt_pk_f32_fp8_e32 v[130:131], v69
	v_cvt_pk_f32_fp8_sdwa v[68:69], v69 src0_sel:WORD_1
	v_cvt_pk_f32_fp8_sdwa v[140:141], v62 src0_sel:WORD_1
	v_cvt_pk_f32_fp8_e32 v[138:139], v62
	v_cvt_pk_f32_fp8_e32 v[142:143], v63
	v_cvt_pk_f32_fp8_sdwa v[62:63], v63 src0_sel:WORD_1
	v_cvt_pk_f32_fp8_sdwa v[152:153], v60 src0_sel:WORD_1
	v_pk_fma_f32 v[4:5], v[16:17], s[24:25], v[4:5] op_sel_hi:[1,0,1]
	v_cvt_pk_f32_fp8_e32 v[150:151], v60
	v_cvt_pk_f32_fp8_e32 v[154:155], v61
	v_cvt_pk_f32_fp8_sdwa v[60:61], v61 src0_sel:WORD_1
	v_cvt_pk_f32_fp8_sdwa v[164:165], v56 src0_sel:WORD_1
	v_pk_fma_f32 v[2:3], v[116:117], s[24:25], v[2:3] op_sel_hi:[1,0,1]
	v_cvt_pk_f32_fp8_e32 v[156:157], v58
	v_cvt_pk_f32_fp8_sdwa v[158:159], v58 src0_sel:WORD_1
	v_cvt_pk_f32_fp8_e32 v[160:161], v59
	v_cvt_pk_f32_fp8_sdwa v[162:163], v59 src0_sel:WORD_1
	v_cvt_pk_f32_fp8_e32 v[58:59], v56
	v_cvt_pk_f32_fp8_e32 v[166:167], v57
	v_cvt_pk_f32_fp8_sdwa v[56:57], v57 src0_sel:WORD_1
	v_cvt_pk_f32_fp8_sdwa v[176:177], v52 src0_sel:WORD_1
	v_pk_fma_f32 v[4:5], v[72:73], s[24:25], v[4:5] op_sel_hi:[1,0,1]
	v_pk_fma_f32 v[2:3], v[128:129], s[24:25], v[2:3] op_sel_hi:[1,0,1]
	v_cvt_pk_f32_fp8_e32 v[168:169], v54
	v_cvt_pk_f32_fp8_sdwa v[170:171], v54 src0_sel:WORD_1
	v_cvt_pk_f32_fp8_e32 v[172:173], v55
	v_cvt_pk_f32_fp8_sdwa v[174:175], v55 src0_sel:WORD_1
	v_cvt_pk_f32_fp8_e32 v[54:55], v52
	v_cvt_pk_f32_fp8_e32 v[178:179], v53
	v_cvt_pk_f32_fp8_sdwa v[52:53], v53 src0_sel:WORD_1
	v_cvt_pk_f32_fp8_sdwa v[188:189], v48 src0_sel:WORD_1
	v_pk_fma_f32 v[4:5], v[68:69], s[24:25], v[4:5] op_sel_hi:[1,0,1]
	v_pk_fma_f32 v[2:3], v[140:141], s[24:25], v[2:3] op_sel_hi:[1,0,1]
	v_pk_fma_f32 v[4:5], v[62:63], s[24:25], v[4:5] op_sel_hi:[1,0,1]
	v_pk_fma_f32 v[2:3], v[152:153], s[24:25], v[2:3] op_sel_hi:[1,0,1]
	v_pk_fma_f32 v[76:77], v[76:77], s[10:11], v[84:85] op_sel_hi:[1,0,1]
	v_pk_fma_f32 v[4:5], v[60:61], s[24:25], v[4:5] op_sel_hi:[1,0,1]
	v_pk_fma_f32 v[2:3], v[164:165], s[24:25], v[2:3] op_sel_hi:[1,0,1]
	s_add_i32 s12, s14, s2
	v_pk_fma_f32 v[6:7], v[6:7], s[24:25], v[76:77] op_sel_hi:[1,0,1]
	v_pk_fma_f32 v[4:5], v[56:57], s[24:25], v[4:5] op_sel_hi:[1,0,1]
	v_pk_fma_f32 v[2:3], v[176:177], s[24:25], v[2:3] op_sel_hi:[1,0,1]
	s_cmpk_lt_i32 s12, 0x4000
	v_pk_fma_f32 v[4:5], v[52:53], s[24:25], v[4:5] op_sel_hi:[1,0,1]
	v_pk_fma_f32 v[52:53], v[188:189], s[24:25], v[2:3] op_sel_hi:[1,0,1]
	v_pk_fma_f32 v[2:3], v[118:119], s[24:25], v[6:7] op_sel_hi:[1,0,1]
	s_cselect_b64 s[16:17], -1, 0
	v_pk_fma_f32 v[2:3], v[130:131], s[24:25], v[2:3] op_sel_hi:[1,0,1]
	s_and_b64 s[18:19], s[16:17], exec
	v_cvt_pk_f32_fp8_e32 v[190:191], v49
	v_pk_fma_f32 v[2:3], v[142:143], s[24:25], v[2:3] op_sel_hi:[1,0,1]
	s_cselect_b32 s18, s12, s14
	v_pk_fma_f32 v[2:3], v[154:155], s[24:25], v[2:3] op_sel_hi:[1,0,1]
	s_ashr_i32 s19, s18, 31
	v_pk_fma_f32 v[2:3], v[166:167], s[24:25], v[2:3] op_sel_hi:[1,0,1]
	s_lshl_b64 s[26:27], s[18:19], 13
	v_pk_fma_f32 v[2:3], v[178:179], s[24:25], v[2:3] op_sel_hi:[1,0,1]
	v_lshl_add_u64 v[18:19], v[34:35], 0, s[26:27]
	v_pk_fma_f32 v[6:7], v[190:191], s[24:25], v[2:3] op_sel_hi:[1,0,1]
	v_pk_fma_f32 v[2:3], v[8:9], s[24:25], v[10:11] op_sel_hi:[1,0,1]
	global_load_dwordx2 v[110:111], v[18:19], off
	global_load_dwordx2 v[108:109], v[18:19], off offset:512
	global_load_dwordx2 v[106:107], v[18:19], off offset:1024
	global_load_dwordx2 v[104:105], v[18:19], off offset:1536
	global_load_dwordx2 v[102:103], v[18:19], off offset:2048
	global_load_dwordx2 v[100:101], v[18:19], off offset:2560
	global_load_dwordx2 v[98:99], v[18:19], off offset:3072
	global_load_dwordx2 v[96:97], v[18:19], off offset:3584
	v_add_co_u32_e32 v18, vcc, s85, v18
	v_pk_fma_f32 v[2:3], v[126:127], s[24:25], v[2:3] op_sel_hi:[1,0,1]
	s_nop 0
	v_addc_co_u32_e32 v19, vcc, 0, v19, vcc
	v_cvt_pk_f32_fp8_e32 v[186:187], v48
	v_cvt_pk_f32_fp8_sdwa v[48:49], v49 src0_sel:WORD_1
	v_pk_fma_f32 v[2:3], v[138:139], s[24:25], v[2:3] op_sel_hi:[1,0,1]
	global_load_dwordx2 v[94:95], v[18:19], off
	global_load_dwordx2 v[92:93], v[18:19], off offset:512
	global_load_dwordx2 v[90:91], v[18:19], off offset:1024
	global_load_dwordx2 v[88:89], v[18:19], off offset:1536
	global_load_dwordx2 v[86:87], v[18:19], off offset:2048
	global_load_dwordx2 v[82:83], v[18:19], off offset:2560
	global_load_dwordx2 v[80:81], v[18:19], off offset:3072
	global_load_dwordx2 v[78:79], v[18:19], off offset:3584
	v_pk_fma_f32 v[2:3], v[150:151], s[24:25], v[2:3] op_sel_hi:[1,0,1]
	s_lshl_b64 s[18:19], s[18:19], 11
	v_pk_fma_f32 v[2:3], v[58:59], s[24:25], v[2:3] op_sel_hi:[1,0,1]
	v_lshl_add_u64 v[18:19], v[36:37], 0, s[18:19]
	v_lshl_add_u64 v[22:23], v[38:39], 0, s[18:19]
	v_pk_fma_f32 v[2:3], v[54:55], s[24:25], v[2:3] op_sel_hi:[1,0,1]
	global_load_dwordx4 v[26:29], v[18:19], off
	s_nop 0
	global_load_dwordx4 v[18:21], v[18:19], off offset:1024
	s_nop 0
	global_load_dwordx4 v[30:33], v[22:23], off
	s_nop 0
	global_load_dwordx4 v[22:25], v[22:23], off offset:1024
	v_pk_fma_f32 v[48:49], v[48:49], s[24:25], v[4:5] op_sel_hi:[1,0,1]
	v_pk_fma_f32 v[62:63], v[186:187], s[24:25], v[2:3] op_sel_hi:[1,0,1]
	v_mov_b64_e32 v[2:3], v[192:193]
	v_mov_b64_e32 v[4:5], v[194:195]
	v_mov_b64_e32 v[8:9], v[196:197]
	v_mov_b64_e32 v[10:11], v[198:199]
	v_mov_b64_e32 v[54:55], v[208:209]
	v_mov_b64_e32 v[56:57], v[210:211]
	v_mov_b64_e32 v[58:59], v[212:213]
	v_mov_b64_e32 v[60:61], v[214:215]
	v_cvt_pk_f32_fp8_e32 v[16:17], v74
	v_cvt_pk_f32_fp8_sdwa v[76:77], v74 src0_sel:WORD_1
	v_cvt_pk_f32_fp8_e32 v[84:85], v75
	v_cvt_pk_f32_fp8_sdwa v[74:75], v75 src0_sel:WORD_1
	v_cvt_pk_f32_fp8_e32 v[120:121], v70
	v_cvt_pk_f32_fp8_sdwa v[122:123], v70 src0_sel:WORD_1
	v_cvt_pk_f32_fp8_e32 v[124:125], v71
	v_cvt_pk_f32_fp8_sdwa v[70:71], v71 src0_sel:WORD_1
	v_cvt_pk_f32_fp8_e32 v[132:133], v66
	v_cvt_pk_f32_fp8_sdwa v[134:135], v66 src0_sel:WORD_1
	v_cvt_pk_f32_fp8_e32 v[136:137], v67
	v_cvt_pk_f32_fp8_sdwa v[66:67], v67 src0_sel:WORD_1
	v_cvt_pk_f32_fp8_e32 v[144:145], v64
	v_cvt_pk_f32_fp8_sdwa v[146:147], v64 src0_sel:WORD_1
	v_cvt_pk_f32_fp8_e32 v[148:149], v65
	v_cvt_pk_f32_fp8_sdwa v[64:65], v65 src0_sel:WORD_1
	v_pk_fma_f32 v[12:13], v[74:75], s[24:25], v[12:13] op_sel_hi:[1,0,1]
	v_cvt_pk_f32_fp8_e32 v[180:181], v50
	v_pk_fma_f32 v[12:13], v[70:71], s[24:25], v[12:13] op_sel_hi:[1,0,1]
	v_cvt_pk_f32_fp8_sdwa v[182:183], v50 src0_sel:WORD_1
	v_cvt_pk_f32_fp8_e32 v[184:185], v51
	v_cvt_pk_f32_fp8_sdwa v[50:51], v51 src0_sel:WORD_1
	v_pk_fma_f32 v[12:13], v[66:67], s[24:25], v[12:13] op_sel_hi:[1,0,1]
	v_pk_fma_f32 v[16:17], v[16:17], s[24:25], v[112:113] op_sel_hi:[1,0,1]
	v_pk_fma_f32 v[12:13], v[64:65], s[24:25], v[12:13] op_sel_hi:[1,0,1]
	v_pk_fma_f32 v[16:17], v[120:121], s[24:25], v[16:17] op_sel_hi:[1,0,1]
	v_pk_fma_f32 v[12:13], v[162:163], s[24:25], v[12:13] op_sel_hi:[1,0,1]
	v_pk_fma_f32 v[14:15], v[76:77], s[24:25], v[14:15] op_sel_hi:[1,0,1]
	v_pk_fma_f32 v[16:17], v[132:133], s[24:25], v[16:17] op_sel_hi:[1,0,1]
	v_pk_fma_f32 v[12:13], v[174:175], s[24:25], v[12:13] op_sel_hi:[1,0,1]
	v_pk_fma_f32 v[14:15], v[122:123], s[24:25], v[14:15] op_sel_hi:[1,0,1]
	v_pk_fma_f32 v[16:17], v[144:145], s[24:25], v[16:17] op_sel_hi:[1,0,1]
	v_pk_fma_f32 v[12:13], v[50:51], s[24:25], v[12:13] op_sel_hi:[1,0,1]
	v_pk_fma_f32 v[14:15], v[134:135], s[24:25], v[14:15] op_sel_hi:[1,0,1]
	v_pk_fma_f32 v[50:51], v[84:85], s[24:25], v[114:115] op_sel_hi:[1,0,1]
	v_pk_fma_f32 v[16:17], v[156:157], s[24:25], v[16:17] op_sel_hi:[1,0,1]
	v_pk_fma_f32 v[14:15], v[146:147], s[24:25], v[14:15] op_sel_hi:[1,0,1]
	v_pk_fma_f32 v[50:51], v[124:125], s[24:25], v[50:51] op_sel_hi:[1,0,1]
	v_pk_fma_f32 v[16:17], v[168:169], s[24:25], v[16:17] op_sel_hi:[1,0,1]
	v_pk_fma_f32 v[14:15], v[158:159], s[24:25], v[14:15] op_sel_hi:[1,0,1]
	v_pk_fma_f32 v[50:51], v[136:137], s[24:25], v[50:51] op_sel_hi:[1,0,1]
	v_pk_fma_f32 v[16:17], v[180:181], s[24:25], v[16:17] op_sel_hi:[1,0,1]
	v_pk_fma_f32 v[14:15], v[170:171], s[24:25], v[14:15] op_sel_hi:[1,0,1]
	v_pk_fma_f32 v[50:51], v[148:149], s[24:25], v[50:51] op_sel_hi:[1,0,1]
	v_add_f32_e32 v0, 0, v16
	v_pk_fma_f32 v[14:15], v[182:183], s[24:25], v[14:15] op_sel_hi:[1,0,1]
	v_pk_fma_f32 v[50:51], v[160:161], s[24:25], v[50:51] op_sel_hi:[1,0,1]
	v_add_f32_e32 v0, v17, v0
	v_pk_fma_f32 v[50:51], v[172:173], s[24:25], v[50:51] op_sel_hi:[1,0,1]
	v_add_f32_e32 v0, v14, v0
	v_pk_fma_f32 v[50:51], v[184:185], s[24:25], v[50:51] op_sel_hi:[1,0,1]
	v_add_f32_e32 v0, v15, v0
	v_add_f32_e32 v0, v50, v0
	v_add_f32_e32 v0, v51, v0
	v_add_f32_e32 v0, v12, v0
	v_add_f32_e32 v0, v13, v0
	v_add_f32_e32 v0, v62, v0
	v_add_f32_e32 v0, v63, v0
	v_add_f32_e32 v0, v52, v0
	v_add_f32_e32 v0, v53, v0
	v_add_f32_e32 v0, v6, v0
	v_add_f32_e32 v0, v7, v0
	v_add_f32_e32 v0, v48, v0
	v_add_f32_e32 v0, v49, v0
	s_ashr_i32 s15, s14, 31
	s_nop 0
	v_add_f32_dpp v0, v0, v0 quad_perm:[1,0,3,2] row_mask:0xf bank_mask:0xf bound_ctrl:1
	s_nop 1
	v_add_f32_dpp v0, v0, v0 quad_perm:[2,3,0,1] row_mask:0xf bank_mask:0xf bound_ctrl:1
	s_nop 1
	v_add_f32_dpp v0, v0, v0 row_half_mirror row_mask:0xf bank_mask:0xf bound_ctrl:1
	s_nop 1
	v_add_f32_dpp v0, v0, v0 row_mirror row_mask:0xf bank_mask:0xf bound_ctrl:1
	s_nop 0
	v_readlane_b32 s11, v0, 16
	v_readlane_b32 s13, v0, 48
	v_readlane_b32 s18, v0, 0
	v_readlane_b32 s19, v0, 32
	v_mov_b32_e32 v64, s11
	v_mov_b32_e32 v65, s13
	v_pk_add_f32 v[64:65], s[18:19], v[64:65]
	s_nop 0
	v_add_f32_e32 v0, v64, v65
	v_mul_f32_e32 v0, 0x3a800000, v0
	v_pk_add_f32 v[64:65], v[16:17], v[0:1] op_sel_hi:[1,0] neg_lo:[0,1] neg_hi:[0,1]
	v_pk_add_f32 v[68:69], v[14:15], v[0:1] op_sel_hi:[1,0] neg_lo:[0,1] neg_hi:[0,1]
	v_pk_mul_f32 v[66:67], v[64:65], v[64:65]
	v_pk_mul_f32 v[70:71], v[68:69], v[68:69]
	v_pk_add_f32 v[72:73], v[50:51], v[0:1] op_sel_hi:[1,0] neg_lo:[0,1] neg_hi:[0,1]
	v_pk_add_f32 v[74:75], v[12:13], v[0:1] op_sel_hi:[1,0] neg_lo:[0,1] neg_hi:[0,1]
	v_pk_add_f32 v[12:13], v[62:63], v[0:1] op_sel_hi:[1,0] neg_lo:[0,1] neg_hi:[0,1]
	v_pk_add_f32 v[14:15], v[52:53], v[0:1] op_sel_hi:[1,0] neg_lo:[0,1] neg_hi:[0,1]
	v_pk_add_f32 v[16:17], v[6:7], v[0:1] op_sel_hi:[1,0] neg_lo:[0,1] neg_hi:[0,1]
	v_pk_add_f32 v[48:49], v[48:49], v[0:1] op_sel_hi:[1,0] neg_lo:[0,1] neg_hi:[0,1]
	v_add_f32_e32 v0, v66, v67
	v_add_f32_e32 v0, v70, v0
	v_pk_mul_f32 v[50:51], v[72:73], v[72:73]
	v_add_f32_e32 v0, v71, v0
	v_add_f32_e32 v0, v50, v0
	v_pk_mul_f32 v[76:77], v[74:75], v[74:75]
	v_add_f32_e32 v0, v51, v0
	v_add_f32_e32 v0, v76, v0
	v_pk_mul_f32 v[62:63], v[12:13], v[12:13]
	v_add_f32_e32 v0, v77, v0
	v_add_f32_e32 v0, v62, v0
	v_pk_mul_f32 v[52:53], v[14:15], v[14:15]
	v_add_f32_e32 v0, v63, v0
	v_add_f32_e32 v0, v52, v0
	v_pk_mul_f32 v[6:7], v[16:17], v[16:17]
	v_add_f32_e32 v0, v53, v0
	v_add_f32_e32 v0, v6, v0
	v_pk_mul_f32 v[84:85], v[48:49], v[48:49]
	v_add_f32_e32 v0, v7, v0
	v_add_f32_e32 v0, v84, v0
	v_add_f32_e32 v0, v85, v0
	s_nop 1
	v_add_f32_dpp v0, v0, v0 quad_perm:[1,0,3,2] row_mask:0xf bank_mask:0xf bound_ctrl:1
	s_nop 1
	v_add_f32_dpp v0, v0, v0 quad_perm:[2,3,0,1] row_mask:0xf bank_mask:0xf bound_ctrl:1
	s_nop 1
	v_add_f32_dpp v0, v0, v0 row_half_mirror row_mask:0xf bank_mask:0xf bound_ctrl:1
	s_nop 1
	v_add_f32_dpp v0, v0, v0 row_mirror row_mask:0xf bank_mask:0xf bound_ctrl:1
	s_nop 0
	v_readlane_b32 s11, v0, 16
	v_readlane_b32 s13, v0, 48
	v_readlane_b32 s18, v0, 0
	v_readlane_b32 s19, v0, 32
	v_mov_b32_e32 v6, s11
	v_mov_b32_e32 v7, s13
	v_pk_add_f32 v[6:7], s[18:19], v[6:7]
	s_lshl_b64 s[18:19], s[14:15], 12
	v_add_f32_e32 v0, v6, v7
	v_fmamk_f32 v0, v0, 0x3a800000, v223
	v_mul_f32_e32 v6, 0x4b800000, v0
	v_cmp_gt_f32_e32 vcc, s80, v0
	v_lshl_add_u64 v[50:51], v[44:45], 0, s[18:19]
	v_readlane_b32 s18, v254, 63
	v_cndmask_b32_e32 v0, v0, v6, vcc
	v_rsq_f32_e32 v0, v0
	v_readlane_b32 s19, v255, 0
	v_mul_f32_e32 v6, 0x45800000, v0
	v_cndmask_b32_e32 v52, v0, v6, vcc
	v_pk_mul_f32 v[6:7], v[64:65], v[52:53] op_sel_hi:[1,0]
	s_and_b64 vcc, exec, s[18:19]
	v_pk_fma_f32 v[6:7], v[2:3], v[6:7], v[54:55]
	v_pk_mul_f32 v[2:3], v[72:73], v[52:53] op_sel_hi:[1,0]
	s_mov_b64 s[18:19], -1
	v_pk_fma_f32 v[2:3], v[8:9], v[2:3], v[58:59]
	v_pk_mul_f32 v[8:9], v[68:69], v[52:53] op_sel_hi:[1,0]
	s_nop 0
	v_pk_fma_f32 v[8:9], v[4:5], v[8:9], v[56:57]
	v_pk_mul_f32 v[4:5], v[74:75], v[52:53] op_sel_hi:[1,0]
	s_nop 0
	v_pk_fma_f32 v[4:5], v[10:11], v[4:5], v[60:61]
	s_cbranch_vccnz .LBB0_1518
	s_mov_b64 s[18:19], 0
	global_store_dwordx4 v[50:51], v[6:9], off
	global_store_dwordx4 v[50:51], v[2:5], off offset:16

.LBB0_1520:
	v_mov_b64_e32 v[2:3], v[204:205]
	v_mov_b64_e32 v[4:5], v[206:207]
	v_mov_b64_e32 v[6:7], v[200:201]
	v_mov_b64_e32 v[8:9], v[202:203]
	s_nop 0
	v_mov_b64_e32 v[56:57], v[216:217]
	v_mov_b64_e32 v[58:59], v[218:219]
	v_mov_b64_e32 v[60:61], v[240:241]
	v_mov_b64_e32 v[62:63], v[242:243]
	v_mov_b32_e32 v53, v52
	v_readlane_b32 s18, v254, 63
	v_readlane_b32 s19, v255, 0
	v_pk_mul_f32 v[12:13], v[12:13], v[52:53]
	v_pk_mul_f32 v[16:17], v[16:17], v[52:53]
	v_pk_mul_f32 v[14:15], v[14:15], v[52:53]
	v_pk_mul_f32 v[48:49], v[48:49], v[52:53]
	s_and_b64 vcc, exec, s[18:19]
	s_mov_b64 s[18:19], -1
	v_pk_fma_f32 v[6:7], v[12:13], v[6:7], v[56:57]
	v_pk_fma_f32 v[2:3], v[16:17], v[2:3], v[60:61]
	v_pk_fma_f32 v[8:9], v[14:15], v[8:9], v[58:59]
	v_pk_fma_f32 v[4:5], v[48:49], v[4:5], v[62:63]
	s_cbranch_vccnz .LBB0_1522
	s_mov_b64 s[18:19], 0
	global_store_dwordx4 v[50:51], v[6:9], off offset:2048
	global_store_dwordx4 v[50:51], v[2:5], off offset:2064

.LBB0_1524:
	s_add_i32 s11, s3, s14
	s_cmpk_lt_i32 s11, 0x4000
	s_cselect_b32 s14, s11, s14
	s_ashr_i32 s15, s14, 31
	s_lshl_b64 s[18:19], s[14:15], 13
	v_lshl_add_u64 v[2:3], v[34:35], 0, s[18:19]
	global_load_dwordx2 v[84:85], v[2:3], off
	global_load_dwordx2 v[76:77], v[2:3], off offset:512
	global_load_dwordx2 v[74:75], v[2:3], off offset:1024
	global_load_dwordx2 v[72:73], v[2:3], off offset:1536
	global_load_dwordx2 v[70:71], v[2:3], off offset:2048
	global_load_dwordx2 v[68:69], v[2:3], off offset:2560
	global_load_dwordx2 v[66:67], v[2:3], off offset:3072
	global_load_dwordx2 v[62:63], v[2:3], off offset:3584
	v_add_co_u32_e32 v2, vcc, s85, v2
	s_lshl_b64 s[14:15], s[14:15], 11
	s_nop 0
	v_addc_co_u32_e32 v3, vcc, 0, v3, vcc
	global_load_dwordx2 v[64:65], v[2:3], off
	global_load_dwordx2 v[60:61], v[2:3], off offset:512
	global_load_dwordx2 v[58:59], v[2:3], off offset:1024
	global_load_dwordx2 v[56:57], v[2:3], off offset:1536
	global_load_dwordx2 v[54:55], v[2:3], off offset:2048
	global_load_dwordx2 v[52:53], v[2:3], off offset:2560
	global_load_dwordx2 v[50:51], v[2:3], off offset:3072
	global_load_dwordx2 v[48:49], v[2:3], off offset:3584
	v_lshl_add_u64 v[2:3], v[36:37], 0, s[14:15]
	v_lshl_add_u64 v[6:7], v[38:39], 0, s[14:15]
	global_load_dwordx4 v[10:13], v[2:3], off
	s_nop 0
	global_load_dwordx4 v[2:5], v[2:3], off offset:1024
	s_nop 0
	global_load_dwordx4 v[14:17], v[6:7], off
	s_nop 0
	global_load_dwordx4 v[6:9], v[6:7], off offset:1024
	s_andn2_b64 vcc, exec, s[16:17]
	s_cbranch_vccnz .LBB0_1515
	s_waitcnt vmcnt(24)
	v_cvt_pk_f32_fp8_sdwa v[114:115], v110 src0_sel:WORD_1
	v_cvt_pk_f32_fp8_e32 v[112:113], v110
	v_lshlrev_b32_e32 v116, 16, v30
	v_and_b32_e32 v117, 0xffff0000, v30
	v_lshlrev_b32_e32 v118, 16, v26
	v_and_b32_e32 v119, 0xffff0000, v26
	v_lshlrev_b32_e32 v30, 16, v31
	v_and_b32_e32 v31, 0xffff0000, v31
	v_lshlrev_b32_e32 v26, 16, v27
	v_and_b32_e32 v27, 0xffff0000, v27
	v_pk_fma_f32 v[26:27], v[30:31], s[10:11], v[26:27] op_sel_hi:[1,0,1]
	v_pk_fma_f32 v[116:117], v[116:117], s[10:11], v[118:119] op_sel_hi:[1,0,1]
	v_pk_fma_f32 v[30:31], v[114:115], s[24:25], v[26:27] op_sel_hi:[1,0,1]
	v_cvt_pk_f32_fp8_e32 v[26:27], v111
	v_pk_fma_f32 v[112:113], v[112:113], s[24:25], v[116:117] op_sel_hi:[1,0,1]
	v_cvt_pk_f32_fp8_sdwa v[110:111], v111 src0_sel:WORD_1
	v_lshlrev_b32_e32 v114, 16, v32
	v_and_b32_e32 v115, 0xffff0000, v32
	v_lshlrev_b32_e32 v116, 16, v28
	v_and_b32_e32 v117, 0xffff0000, v28
	v_pk_fma_f32 v[114:115], v[114:115], s[10:11], v[116:117] op_sel_hi:[1,0,1]
	v_lshlrev_b32_e32 v28, 16, v29
	v_pk_fma_f32 v[114:115], v[26:27], s[24:25], v[114:115] op_sel_hi:[1,0,1]
	v_lshlrev_b32_e32 v26, 16, v33
	v_and_b32_e32 v27, 0xffff0000, v33
	v_and_b32_e32 v29, 0xffff0000, v29
	v_pk_fma_f32 v[26:27], v[26:27], s[10:11], v[28:29] op_sel_hi:[1,0,1]
	v_cvt_pk_f32_fp8_sdwa v[32:33], v108 src0_sel:WORD_1
	v_pk_fma_f32 v[28:29], v[110:111], s[24:25], v[26:27] op_sel_hi:[1,0,1]
	v_cvt_pk_f32_fp8_e32 v[26:27], v108
	v_lshlrev_b32_e32 v110, 16, v22
	v_and_b32_e32 v111, 0xffff0000, v22
	v_lshlrev_b32_e32 v116, 16, v18
	v_and_b32_e32 v117, 0xffff0000, v18
	v_lshlrev_b32_e32 v22, 16, v23
	v_and_b32_e32 v23, 0xffff0000, v23
	v_lshlrev_b32_e32 v18, 16, v19
	v_and_b32_e32 v19, 0xffff0000, v19
	v_pk_fma_f32 v[110:111], v[110:111], s[10:11], v[116:117] op_sel_hi:[1,0,1]
	v_pk_fma_f32 v[18:19], v[22:23], s[10:11], v[18:19] op_sel_hi:[1,0,1]
	v_pk_fma_f32 v[26:27], v[26:27], s[24:25], v[110:111] op_sel_hi:[1,0,1]
	v_pk_fma_f32 v[18:19], v[32:33], s[24:25], v[18:19] op_sel_hi:[1,0,1]
	v_cvt_pk_f32_fp8_e32 v[22:23], v109
	v_cvt_pk_f32_fp8_sdwa v[32:33], v109 src0_sel:WORD_1
	v_lshlrev_b32_e32 v108, 16, v24
	v_and_b32_e32 v109, 0xffff0000, v24
	v_lshlrev_b32_e32 v110, 16, v20
	v_and_b32_e32 v111, 0xffff0000, v20
	v_lshlrev_b32_e32 v24, 16, v25
	v_and_b32_e32 v25, 0xffff0000, v25
	v_lshlrev_b32_e32 v20, 16, v21
	v_and_b32_e32 v21, 0xffff0000, v21
	v_cvt_pk_f32_fp8_sdwa v[116:117], v104 src0_sel:WORD_1
	v_pk_fma_f32 v[20:21], v[24:25], s[10:11], v[20:21] op_sel_hi:[1,0,1]
	v_cvt_pk_f32_fp8_e32 v[24:25], v104
	v_cvt_pk_f32_fp8_e32 v[118:119], v105
	v_cvt_pk_f32_fp8_sdwa v[104:105], v105 src0_sel:WORD_1
	v_cvt_pk_f32_fp8_sdwa v[128:129], v100 src0_sel:WORD_1
	v_cvt_pk_f32_fp8_e32 v[126:127], v100
	v_cvt_pk_f32_fp8_e32 v[130:131], v101
	v_cvt_pk_f32_fp8_sdwa v[100:101], v101 src0_sel:WORD_1
	v_cvt_pk_f32_fp8_sdwa v[140:141], v96 src0_sel:WORD_1
	v_cvt_pk_f32_fp8_e32 v[138:139], v96
	v_cvt_pk_f32_fp8_e32 v[142:143], v97
	v_cvt_pk_f32_fp8_sdwa v[96:97], v97 src0_sel:WORD_1
	v_cvt_pk_f32_fp8_sdwa v[152:153], v92 src0_sel:WORD_1
	v_pk_fma_f32 v[20:21], v[32:33], s[24:25], v[20:21] op_sel_hi:[1,0,1]
	v_cvt_pk_f32_fp8_e32 v[150:151], v92
	v_cvt_pk_f32_fp8_e32 v[154:155], v93
	v_cvt_pk_f32_fp8_sdwa v[92:93], v93 src0_sel:WORD_1
	v_cvt_pk_f32_fp8_sdwa v[164:165], v88 src0_sel:WORD_1
	v_pk_fma_f32 v[18:19], v[116:117], s[24:25], v[18:19] op_sel_hi:[1,0,1]
	v_cvt_pk_f32_fp8_e32 v[156:157], v90
	v_cvt_pk_f32_fp8_sdwa v[158:159], v90 src0_sel:WORD_1
	v_cvt_pk_f32_fp8_e32 v[160:161], v91
	v_cvt_pk_f32_fp8_sdwa v[162:163], v91 src0_sel:WORD_1
	v_cvt_pk_f32_fp8_e32 v[90:91], v88
	v_cvt_pk_f32_fp8_e32 v[166:167], v89
	v_cvt_pk_f32_fp8_sdwa v[88:89], v89 src0_sel:WORD_1
	v_cvt_pk_f32_fp8_sdwa v[176:177], v82 src0_sel:WORD_1
	v_pk_fma_f32 v[20:21], v[104:105], s[24:25], v[20:21] op_sel_hi:[1,0,1]
	v_pk_fma_f32 v[18:19], v[128:129], s[24:25], v[18:19] op_sel_hi:[1,0,1]
	v_cvt_pk_f32_fp8_e32 v[168:169], v86
	v_cvt_pk_f32_fp8_sdwa v[170:171], v86 src0_sel:WORD_1
	v_cvt_pk_f32_fp8_e32 v[172:173], v87
	v_cvt_pk_f32_fp8_sdwa v[174:175], v87 src0_sel:WORD_1
	v_cvt_pk_f32_fp8_e32 v[86:87], v82
	v_cvt_pk_f32_fp8_e32 v[178:179], v83
	v_cvt_pk_f32_fp8_sdwa v[82:83], v83 src0_sel:WORD_1
	v_cvt_pk_f32_fp8_sdwa v[188:189], v78 src0_sel:WORD_1
	v_pk_fma_f32 v[20:21], v[100:101], s[24:25], v[20:21] op_sel_hi:[1,0,1]
	v_pk_fma_f32 v[18:19], v[140:141], s[24:25], v[18:19] op_sel_hi:[1,0,1]
	v_pk_fma_f32 v[20:21], v[96:97], s[24:25], v[20:21] op_sel_hi:[1,0,1]
	v_pk_fma_f32 v[18:19], v[152:153], s[24:25], v[18:19] op_sel_hi:[1,0,1]
	v_pk_fma_f32 v[108:109], v[108:109], s[10:11], v[110:111] op_sel_hi:[1,0,1]
	v_pk_fma_f32 v[20:21], v[92:93], s[24:25], v[20:21] op_sel_hi:[1,0,1]
	v_pk_fma_f32 v[18:19], v[164:165], s[24:25], v[18:19] op_sel_hi:[1,0,1]
	v_pk_fma_f32 v[22:23], v[22:23], s[24:25], v[108:109] op_sel_hi:[1,0,1]
	v_pk_fma_f32 v[20:21], v[88:89], s[24:25], v[20:21] op_sel_hi:[1,0,1]
	v_pk_fma_f32 v[18:19], v[176:177], s[24:25], v[18:19] op_sel_hi:[1,0,1]
	v_pk_fma_f32 v[20:21], v[82:83], s[24:25], v[20:21] op_sel_hi:[1,0,1]
	v_pk_fma_f32 v[82:83], v[188:189], s[24:25], v[18:19] op_sel_hi:[1,0,1]
	v_pk_fma_f32 v[18:19], v[118:119], s[24:25], v[22:23] op_sel_hi:[1,0,1]
	v_cvt_pk_f32_fp8_e32 v[190:191], v79
	v_pk_fma_f32 v[18:19], v[130:131], s[24:25], v[18:19] op_sel_hi:[1,0,1]
	v_cvt_pk_f32_fp8_e32 v[186:187], v78
	v_pk_fma_f32 v[18:19], v[142:143], s[24:25], v[18:19] op_sel_hi:[1,0,1]
	v_cvt_pk_f32_fp8_sdwa v[78:79], v79 src0_sel:WORD_1
	v_pk_fma_f32 v[18:19], v[154:155], s[24:25], v[18:19] op_sel_hi:[1,0,1]
	v_cvt_pk_f32_fp8_e32 v[32:33], v106
	v_pk_fma_f32 v[18:19], v[166:167], s[24:25], v[18:19] op_sel_hi:[1,0,1]
	v_pk_fma_f32 v[78:79], v[78:79], s[24:25], v[20:21] op_sel_hi:[1,0,1]
	v_pk_fma_f32 v[18:19], v[178:179], s[24:25], v[18:19] op_sel_hi:[1,0,1]
	v_cvt_pk_f32_fp8_sdwa v[108:109], v106 src0_sel:WORD_1
	v_pk_fma_f32 v[96:97], v[190:191], s[24:25], v[18:19] op_sel_hi:[1,0,1]
	v_pk_fma_f32 v[18:19], v[24:25], s[24:25], v[26:27] op_sel_hi:[1,0,1]
	v_cvt_pk_f32_fp8_e32 v[110:111], v107
	v_pk_fma_f32 v[18:19], v[126:127], s[24:25], v[18:19] op_sel_hi:[1,0,1]
	v_cvt_pk_f32_fp8_sdwa v[106:107], v107 src0_sel:WORD_1
	v_pk_fma_f32 v[18:19], v[138:139], s[24:25], v[18:19] op_sel_hi:[1,0,1]
	v_cvt_pk_f32_fp8_e32 v[120:121], v102
	v_pk_fma_f32 v[18:19], v[150:151], s[24:25], v[18:19] op_sel_hi:[1,0,1]
	v_cvt_pk_f32_fp8_sdwa v[122:123], v102 src0_sel:WORD_1
	v_pk_fma_f32 v[18:19], v[90:91], s[24:25], v[18:19] op_sel_hi:[1,0,1]
	v_cvt_pk_f32_fp8_e32 v[124:125], v103
	v_pk_fma_f32 v[18:19], v[86:87], s[24:25], v[18:19] op_sel_hi:[1,0,1]
	v_cvt_pk_f32_fp8_sdwa v[102:103], v103 src0_sel:WORD_1
	v_pk_fma_f32 v[100:101], v[186:187], s[24:25], v[18:19] op_sel_hi:[1,0,1]
	v_mov_b64_e32 v[18:19], v[192:193]
	v_mov_b64_e32 v[20:21], v[194:195]
	v_mov_b64_e32 v[86:87], v[196:197]
	v_mov_b64_e32 v[88:89], v[198:199]
	v_mov_b64_e32 v[22:23], v[208:209]
	v_mov_b64_e32 v[24:25], v[210:211]
	v_mov_b64_e32 v[90:91], v[212:213]
	v_mov_b64_e32 v[92:93], v[214:215]
	v_cvt_pk_f32_fp8_e32 v[132:133], v98
	v_cvt_pk_f32_fp8_sdwa v[134:135], v98 src0_sel:WORD_1
	v_cvt_pk_f32_fp8_e32 v[136:137], v99
	v_cvt_pk_f32_fp8_sdwa v[98:99], v99 src0_sel:WORD_1
	v_cvt_pk_f32_fp8_e32 v[144:145], v94
	v_cvt_pk_f32_fp8_sdwa v[146:147], v94 src0_sel:WORD_1
	v_cvt_pk_f32_fp8_e32 v[148:149], v95
	v_cvt_pk_f32_fp8_sdwa v[94:95], v95 src0_sel:WORD_1
	v_pk_fma_f32 v[28:29], v[106:107], s[24:25], v[28:29] op_sel_hi:[1,0,1]
	v_cvt_pk_f32_fp8_e32 v[180:181], v80
	v_pk_fma_f32 v[28:29], v[102:103], s[24:25], v[28:29] op_sel_hi:[1,0,1]
	v_cvt_pk_f32_fp8_sdwa v[182:183], v80 src0_sel:WORD_1
	v_cvt_pk_f32_fp8_e32 v[184:185], v81
	v_cvt_pk_f32_fp8_sdwa v[80:81], v81 src0_sel:WORD_1
	v_pk_fma_f32 v[28:29], v[98:99], s[24:25], v[28:29] op_sel_hi:[1,0,1]
	v_pk_fma_f32 v[32:33], v[32:33], s[24:25], v[112:113] op_sel_hi:[1,0,1]
	v_pk_fma_f32 v[28:29], v[94:95], s[24:25], v[28:29] op_sel_hi:[1,0,1]
	v_pk_fma_f32 v[32:33], v[120:121], s[24:25], v[32:33] op_sel_hi:[1,0,1]
	v_pk_fma_f32 v[28:29], v[162:163], s[24:25], v[28:29] op_sel_hi:[1,0,1]
	v_pk_fma_f32 v[30:31], v[108:109], s[24:25], v[30:31] op_sel_hi:[1,0,1]
	v_pk_fma_f32 v[32:33], v[132:133], s[24:25], v[32:33] op_sel_hi:[1,0,1]
	v_pk_fma_f32 v[28:29], v[174:175], s[24:25], v[28:29] op_sel_hi:[1,0,1]
	v_pk_fma_f32 v[30:31], v[122:123], s[24:25], v[30:31] op_sel_hi:[1,0,1]
	v_pk_fma_f32 v[32:33], v[144:145], s[24:25], v[32:33] op_sel_hi:[1,0,1]
	v_pk_fma_f32 v[28:29], v[80:81], s[24:25], v[28:29] op_sel_hi:[1,0,1]
	v_pk_fma_f32 v[30:31], v[134:135], s[24:25], v[30:31] op_sel_hi:[1,0,1]
	v_pk_fma_f32 v[80:81], v[110:111], s[24:25], v[114:115] op_sel_hi:[1,0,1]
	v_pk_fma_f32 v[32:33], v[156:157], s[24:25], v[32:33] op_sel_hi:[1,0,1]
	v_pk_fma_f32 v[30:31], v[146:147], s[24:25], v[30:31] op_sel_hi:[1,0,1]
	v_pk_fma_f32 v[80:81], v[124:125], s[24:25], v[80:81] op_sel_hi:[1,0,1]
	v_pk_fma_f32 v[32:33], v[168:169], s[24:25], v[32:33] op_sel_hi:[1,0,1]
	v_pk_fma_f32 v[30:31], v[158:159], s[24:25], v[30:31] op_sel_hi:[1,0,1]
	v_pk_fma_f32 v[80:81], v[136:137], s[24:25], v[80:81] op_sel_hi:[1,0,1]
	v_pk_fma_f32 v[32:33], v[180:181], s[24:25], v[32:33] op_sel_hi:[1,0,1]
	v_pk_fma_f32 v[30:31], v[170:171], s[24:25], v[30:31] op_sel_hi:[1,0,1]
	v_pk_fma_f32 v[80:81], v[148:149], s[24:25], v[80:81] op_sel_hi:[1,0,1]
	v_add_f32_e32 v0, 0, v32
	v_pk_fma_f32 v[30:31], v[182:183], s[24:25], v[30:31] op_sel_hi:[1,0,1]
	v_pk_fma_f32 v[80:81], v[160:161], s[24:25], v[80:81] op_sel_hi:[1,0,1]
	v_add_f32_e32 v0, v33, v0
	v_pk_fma_f32 v[80:81], v[172:173], s[24:25], v[80:81] op_sel_hi:[1,0,1]
	v_add_f32_e32 v0, v30, v0
	v_pk_fma_f32 v[80:81], v[184:185], s[24:25], v[80:81] op_sel_hi:[1,0,1]
	v_add_f32_e32 v0, v31, v0
	v_add_f32_e32 v0, v80, v0
	v_add_f32_e32 v0, v81, v0
	v_add_f32_e32 v0, v28, v0
	v_add_f32_e32 v0, v29, v0
	v_add_f32_e32 v0, v100, v0
	v_add_f32_e32 v0, v101, v0
	v_add_f32_e32 v0, v82, v0
	v_add_f32_e32 v0, v83, v0
	v_add_f32_e32 v0, v96, v0
	v_add_f32_e32 v0, v97, v0
	v_add_f32_e32 v0, v78, v0
	v_add_f32_e32 v0, v79, v0
	s_ashr_i32 s13, s12, 31
	s_lshl_b64 s[14:15], s[12:13], 12
	v_add_f32_dpp v0, v0, v0 quad_perm:[1,0,3,2] row_mask:0xf bank_mask:0xf bound_ctrl:1
	v_lshl_add_u64 v[26:27], v[44:45], 0, s[14:15]
	s_nop 0
	v_add_f32_dpp v0, v0, v0 quad_perm:[2,3,0,1] row_mask:0xf bank_mask:0xf bound_ctrl:1
	s_nop 1
	v_add_f32_dpp v0, v0, v0 row_half_mirror row_mask:0xf bank_mask:0xf bound_ctrl:1
	s_nop 1
	v_add_f32_dpp v0, v0, v0 row_mirror row_mask:0xf bank_mask:0xf bound_ctrl:1
	s_nop 0
	v_readlane_b32 s11, v0, 16
	v_readlane_b32 s16, v0, 48
	v_readlane_b32 s14, v0, 0
	v_readlane_b32 s15, v0, 32
	v_mov_b32_e32 v94, s11
	v_mov_b32_e32 v95, s16
	v_pk_add_f32 v[94:95], s[14:15], v[94:95]
	s_nop 0
	v_add_f32_e32 v0, v94, v95
	v_mul_f32_e32 v0, 0x3a800000, v0
	v_pk_add_f32 v[94:95], v[32:33], v[0:1] op_sel_hi:[1,0] neg_lo:[0,1] neg_hi:[0,1]
	v_pk_add_f32 v[102:103], v[30:31], v[0:1] op_sel_hi:[1,0] neg_lo:[0,1] neg_hi:[0,1]
	v_pk_mul_f32 v[98:99], v[94:95], v[94:95]
	v_pk_mul_f32 v[104:105], v[102:103], v[102:103]
	v_pk_add_f32 v[80:81], v[80:81], v[0:1] op_sel_hi:[1,0] neg_lo:[0,1] neg_hi:[0,1]
	v_pk_add_f32 v[108:109], v[28:29], v[0:1] op_sel_hi:[1,0] neg_lo:[0,1] neg_hi:[0,1]
	v_pk_add_f32 v[28:29], v[100:101], v[0:1] op_sel_hi:[1,0] neg_lo:[0,1] neg_hi:[0,1]
	v_pk_add_f32 v[30:31], v[82:83], v[0:1] op_sel_hi:[1,0] neg_lo:[0,1] neg_hi:[0,1]
	v_pk_add_f32 v[32:33], v[96:97], v[0:1] op_sel_hi:[1,0] neg_lo:[0,1] neg_hi:[0,1]
	v_pk_add_f32 v[78:79], v[78:79], v[0:1] op_sel_hi:[1,0] neg_lo:[0,1] neg_hi:[0,1]
	v_add_f32_e32 v0, v98, v99
	v_add_f32_e32 v0, v104, v0
	v_pk_mul_f32 v[106:107], v[80:81], v[80:81]
	v_add_f32_e32 v0, v105, v0
	v_add_f32_e32 v0, v106, v0
	v_pk_mul_f32 v[110:111], v[108:109], v[108:109]
	v_add_f32_e32 v0, v107, v0
	v_add_f32_e32 v0, v110, v0
	v_pk_mul_f32 v[100:101], v[28:29], v[28:29]
	v_add_f32_e32 v0, v111, v0
	v_add_f32_e32 v0, v100, v0
	v_pk_mul_f32 v[82:83], v[30:31], v[30:31]
	v_add_f32_e32 v0, v101, v0
	v_add_f32_e32 v0, v82, v0
	v_pk_mul_f32 v[96:97], v[32:33], v[32:33]
	v_add_f32_e32 v0, v83, v0
	v_add_f32_e32 v0, v96, v0
	v_pk_mul_f32 v[112:113], v[78:79], v[78:79]
	v_add_f32_e32 v0, v97, v0
	v_add_f32_e32 v0, v112, v0
	v_add_f32_e32 v0, v113, v0
	s_nop 1
	v_add_f32_dpp v0, v0, v0 quad_perm:[1,0,3,2] row_mask:0xf bank_mask:0xf bound_ctrl:1
	s_nop 1
	v_add_f32_dpp v0, v0, v0 quad_perm:[2,3,0,1] row_mask:0xf bank_mask:0xf bound_ctrl:1
	s_nop 1
	v_add_f32_dpp v0, v0, v0 row_half_mirror row_mask:0xf bank_mask:0xf bound_ctrl:1
	s_nop 1
	v_add_f32_dpp v0, v0, v0 row_mirror row_mask:0xf bank_mask:0xf bound_ctrl:1
	s_nop 0
	v_readlane_b32 s11, v0, 16
	v_readlane_b32 s16, v0, 48
	v_readlane_b32 s14, v0, 0
	v_readlane_b32 s15, v0, 32
	v_mov_b32_e32 v82, s11
	v_mov_b32_e32 v83, s16
	v_pk_add_f32 v[82:83], s[14:15], v[82:83]
	v_readlane_b32 s16, v254, 63
	v_add_f32_e32 v0, v82, v83
	v_fmamk_f32 v0, v0, 0x3a800000, v223
	v_cmp_gt_f32_e32 vcc, s80, v0
	v_mul_f32_e32 v82, 0x4b800000, v0
	v_readlane_b32 s17, v255, 0
	v_cndmask_b32_e32 v0, v0, v82, vcc
	v_rsq_f32_e32 v0, v0
	s_mov_b64 s[14:15], -1
	v_mul_f32_e32 v82, 0x45800000, v0
	v_cndmask_b32_e32 v82, v0, v82, vcc
	v_pk_mul_f32 v[94:95], v[94:95], v[82:83] op_sel_hi:[1,0]
	s_and_b64 vcc, exec, s[16:17]
	v_pk_fma_f32 v[22:23], v[18:19], v[94:95], v[22:23]
	v_pk_mul_f32 v[18:19], v[80:81], v[82:83] op_sel_hi:[1,0]
	v_pk_mul_f32 v[80:81], v[102:103], v[82:83] op_sel_hi:[1,0]
	v_pk_fma_f32 v[18:19], v[86:87], v[18:19], v[90:91]
	v_pk_fma_f32 v[24:25], v[20:21], v[80:81], v[24:25]
	v_pk_mul_f32 v[20:21], v[108:109], v[82:83] op_sel_hi:[1,0]
	s_nop 0
	v_pk_fma_f32 v[20:21], v[88:89], v[20:21], v[92:93]
	s_cbranch_vccnz .LBB0_1527
	s_mov_b64 s[14:15], 0
	global_store_dwordx4 v[26:27], v[22:25], off
	global_store_dwordx4 v[26:27], v[18:21], off offset:16

.LBB0_1529:
	v_mov_b64_e32 v[18:19], v[204:205]
	v_mov_b64_e32 v[20:21], v[206:207]
	v_mov_b64_e32 v[22:23], v[200:201]
	v_mov_b64_e32 v[24:25], v[202:203]
	s_nop 0
	v_mov_b64_e32 v[88:89], v[216:217]
	v_mov_b64_e32 v[90:91], v[218:219]
	v_mov_b64_e32 v[92:93], v[240:241]
	v_mov_b64_e32 v[94:95], v[242:243]
	v_mov_b32_e32 v83, v82
	v_readlane_b32 s14, v254, 63
	v_readlane_b32 s15, v255, 0
	v_pk_mul_f32 v[28:29], v[28:29], v[82:83]
	v_pk_mul_f32 v[32:33], v[32:33], v[82:83]
	v_pk_mul_f32 v[30:31], v[30:31], v[82:83]
	v_pk_mul_f32 v[78:79], v[78:79], v[82:83]
	s_and_b64 vcc, exec, s[14:15]
	s_mov_b64 s[14:15], -1
	v_pk_fma_f32 v[22:23], v[28:29], v[22:23], v[88:89]
	v_pk_fma_f32 v[18:19], v[32:33], v[18:19], v[92:93]
	v_pk_fma_f32 v[24:25], v[30:31], v[24:25], v[90:91]
	v_pk_fma_f32 v[20:21], v[78:79], v[20:21], v[94:95]
	s_cbranch_vccnz .LBB0_1531
	s_mov_b64 s[14:15], 0
	global_store_dwordx4 v[26:27], v[22:25], off offset:2048
	global_store_dwordx4 v[26:27], v[18:21], off offset:2064
